# v19: v16 + spatial gating: LayerNorm gains and biases through LDS (2 loads per wave instead of 16 per thread)
# speedup vs baseline: 1.0083x; 1.0043x over previous
; #define LAS __attribute__((address_space(3)))
; __device__ __forceinline__ void sg_phase(const Frame& F, const KArgs& a, const int u_first, const int u_count) {
;     unsigned char* ws = F.ws; const int tid = F.tid, lane = F.lane, w = F.wave, tl = lane & 15, kq = lane >> 4;
;     LAS f32x2* st = (LAS f32x2*)F.lds;
;     LAS unsigned short* vt = (LAS unsigned short*)(F.lds + 1024);
;     const bf16* ZU = (const bf16*)(ws + WS_ZU); const bf16* ZV = (const bf16*)(ws + WS_ZV); const float* ZST = (const float*)(ws + WS_ZST); bf16* AS = (bf16*)(ws + WS_AS);
;     const float* ln_g = a.in[5]; const float* ln_b = a.in[6]; const float* w_sp = a.in[7]; const float* b_sp = a.in[8];
;     for (int uu = 0; uu < u_count; ++uu) { const int u = u_first + uu;
;         const int chunk = u >> 3, g = u & 7, t0 = chunk * SGC;
;         const int t = 16 * w + tl;
;         f32x4 zst[8];
;         if (tid < 128) { const f32x4* p = (const f32x4*)(ZST + (size_t)(t0 + tid) * 32);
; #pragma unroll
;             for (int i = 0; i < 8; ++i) zst[i] = p[i]; }
;         const int s_ = tid >> 2, c0 = (tid & 3) * 32; const bf16* src = ZV + (size_t)(t0 + s_) * SGW + g * 128 + c0;
;         u32x4 zraw[4]; f32x4 lg[4][2], lb[4][2];
; #pragma unroll
;         for (int q = 0; q < 4; ++q) { zraw[q] = ((const u32x4*)src)[q];
;             lg[q][0] = *(const f32x4*)(ln_g + g * 128 + c0 + 8 * q); lg[q][1] = *(const f32x4*)(ln_g + g * 128 + c0 + 8 * q + 4); lb[q][0] = *(const f32x4*)(ln_b + g * 128 + c0 + 8 * q); lb[q][1] = *(const f32x4*)(ln_b + g * 128 + c0 + 8 * q + 4); }
;         f32x4 wraw[4][2];
; #pragma unroll
;         for (int ks = 0; ks < 4; ++ks) { const float* wp = w_sp + ((size_t)(g * 128 + t) * 128 + 32 * ks + 8 * kq); if (ks <= (w >> 1)) { wraw[ks][0] = *(const f32x4*)wp; wraw[ks][1] = *(const f32x4*)(wp + 4); } else { wraw[ks][0] = (f32x4){0.f, 0.f, 0.f, 0.f}; wraw[ks][1] = (f32x4){0.f, 0.f, 0.f, 0.f}; } }
;         u32x2 uraw[8];
; #pragma unroll
;         for (int j = 0; j < 8; ++j) uraw[j] = *(const u32x2*)(ZU + (size_t)(t0 + t) * SGW + g * 128 + 16 * j + 4 * kq);
;         const float bs = b_sp[g * 128 + t];
.LBB0_802:
	s_waitcnt vmcnt(0)
	v_lshrrev_b32_e32 v4, 4, v198
	s_waitcnt lgkmcnt(0)
	v_and_b32_e32 v3, 15, v0
	v_readlane_b32 s4, v252, 6
	v_lshlrev_b32_e32 v6, 3, v4
	v_lshl_or_b32 v176, s75, 4, v3
	v_readlane_b32 s8, v252, 10
	v_readlane_b32 s9, v252, 11
	v_or_b32_e32 v8, 2, v6
	v_readlane_b32 s10, v252, 12
	v_readlane_b32 s11, v252, 13
	v_cmp_gt_u32_e64 s[8:9], v8, v176
	v_or_b32_e32 v8, 3, v6
	v_and_b32_e32 v5, 3, v0
	v_readlane_b32 s12, v252, 14
	v_readlane_b32 s13, v252, 15
	v_cmp_gt_u32_e64 s[10:11], v8, v176
	v_or_b32_e32 v8, 4, v6
	v_mov_b32_e32 v147, 0
	v_lshlrev_b32_e32 v146, 7, v5
	v_readlane_b32 s14, v252, 16
	v_readlane_b32 s15, v252, 17
	v_cmp_gt_u32_e64 s[12:13], v8, v176
	v_or_b32_e32 v8, 5, v6
	v_readlane_b32 s16, v252, 18
	v_readlane_b32 s17, v252, 19
	v_lshl_add_u64 v[148:149], s[14:15], 0, v[146:147]
	v_cmp_gt_u32_e64 s[14:15], v8, v176
	v_or_b32_e32 v8, 6, v6
	v_readlane_b32 s18, v252, 20
	v_readlane_b32 s19, v252, 21
	v_lshl_add_u64 v[150:151], s[16:17], 0, v[146:147]
	v_lshlrev_b32_e32 v146, 5, v4
	v_cmp_gt_u32_e64 s[16:17], v8, v176
	v_or_b32_e32 v8, 7, v6
	s_movk_i32 s20, 0x110
	v_lshl_add_u64 v[152:153], s[18:19], 0, v[146:147]
	v_cmp_gt_u32_e64 s[18:19], v8, v176
	v_mad_u32_u24 v3, v3, s20, 0
	v_and_b32_e32 v8, 48, v198
	v_writelane_b32 v251, s71, 13
	v_add_u32_e32 v180, v3, v8
	v_xad_u32 v181, v8, 32, v3
	v_or_b32_e32 v8, 32, v6
	v_writelane_b32 v251, s75, 14
	v_cmp_gt_u32_e64 s[20:21], v8, v176
	v_or_b32_e32 v8, 33, v6
	s_add_u32 s0, s72, 0xb600000
	v_writelane_b32 v251, s20, 7
	s_addc_u32 s1, s73, 0
	s_add_u32 s80, s72, 0xd600000
	v_writelane_b32 v251, s21, 8
	v_cmp_gt_u32_e64 s[20:21], v8, v176
	v_or_b32_e32 v8, 34, v6
	s_addc_u32 s81, s73, 0
	v_writelane_b32 v251, s20, 16
	s_add_u32 s84, s72, 0xf600000
	s_addc_u32 s85, s73, 0
	v_writelane_b32 v251, s21, 17
	v_cmp_gt_u32_e64 s[20:21], v8, v176
	v_or_b32_e32 v8, 35, v6
	v_readlane_b32 s4, v252, 63
	v_writelane_b32 v251, s20, 22
	v_lshrrev_b32_e32 v177, 2, v0
	s_cmpk_gt_u32 s4, 0x7f
	v_writelane_b32 v251, s21, 23
	v_cmp_gt_u32_e64 s[20:21], v8, v176
	v_or_b32_e32 v8, 36, v6
	v_lshlrev_b32_e32 v2, 5, v5
	v_writelane_b32 v251, s20, 24
	v_readlane_b32 s5, v252, 7
	v_readlane_b32 s6, v252, 8
	v_writelane_b32 v251, s21, 25
	v_cmp_gt_u32_e64 s[20:21], v8, v176
	v_or_b32_e32 v8, 37, v6
	v_readlane_b32 s7, v252, 9
	v_writelane_b32 v251, s20, 26
	v_lshlrev_b32_e32 v7, 1, v177
	s_cselect_b64 s[82:83], -1, 0
	v_writelane_b32 v251, s21, 27
	v_cmp_gt_u32_e64 s[20:21], v8, v176
	v_or_b32_e32 v8, 38, v6
	v_cmp_gt_u32_e64 s[34:35], v8, v176
	v_or_b32_e32 v8, 39, v6
	v_cmp_gt_u32_e64 s[94:95], v8, v176
	v_or_b32_e32 v8, 64, v6
	v_writelane_b32 v251, s20, 28
	v_cmp_gt_u32_e64 s[96:97], v8, v176
	v_or_b32_e32 v8, 0x41, v6
	v_writelane_b32 v251, s21, 29
	v_cmp_gt_u32_e64 s[20:21], v8, v176
	v_or_b32_e32 v8, 0x42, v6
	v_cmp_gt_u32_e64 s[22:23], v8, v176
	v_or_b32_e32 v8, 0x43, v6
	v_cmp_gt_u32_e64 s[24:25], v8, v176
	v_or_b32_e32 v8, 0x44, v6
	v_cmp_gt_u32_e64 s[26:27], v8, v176
	v_or_b32_e32 v8, 0x45, v6
	v_cmp_gt_u32_e64 s[28:29], v8, v176
	v_or_b32_e32 v8, 0x46, v6
	v_cmp_gt_u32_e64 s[30:31], v8, v176
	v_or_b32_e32 v8, 0x47, v6
	v_cmp_gt_u32_e64 s[52:53], v8, v176
	v_or_b32_e32 v8, 0x60, v6
	v_cmp_gt_u32_e64 s[54:55], v8, v176
	v_or_b32_e32 v8, 0x61, v6
	v_cmp_gt_u32_e64 s[56:57], v8, v176
	v_or_b32_e32 v8, 0x62, v6
	v_cmp_gt_u32_e64 s[58:59], v8, v176
	v_or_b32_e32 v8, 0x63, v6
	v_cmp_gt_u32_e64 s[60:61], v8, v176
	v_or_b32_e32 v8, 0x64, v6
	v_cmp_gt_u32_e64 s[62:63], v8, v176
	v_or_b32_e32 v8, 0x65, v6
	v_cmp_gt_u32_e64 s[64:65], v8, v176
	v_or_b32_e32 v8, 0x66, v6
	v_cmp_gt_u32_e64 s[66:67], v8, v176
	v_or_b32_e32 v8, 0x67, v6
	s_cmpk_gt_u32 s4, 0xff
	v_cmp_gt_u32_e64 s[68:69], v8, v176
	s_movk_i32 s33, 0x58
	v_mov_b32_e32 v8, 0x60
	s_movk_i32 s2, 0x80
	v_lshlrev_b32_e32 v4, 2, v4
	v_xad_u32 v7, v2, v7, 0
	s_cselect_b64 s[86:87], -1, 0
	s_cmpk_gt_u32 s4, 0x17f
	v_mul_u32_u24_e32 v5, 0x2200, v5
	v_cmp_gt_u32_e64 s[4:5], v6, v176
	v_cmp_lt_u32_e64 s[6:7], v6, v176
	v_bitop3_b32 v6, v6, s33, v8 bitop3:0xc8
	v_cmp_gt_u32_e64 s[2:3], s2, v0
	s_mov_b32 s79, 0
	v_lshl_add_u32 v178, v0, 3, 0
	v_lshl_add_u32 v179, v177, 3, 0
	s_cselect_b64 s[88:89], -1, 0
	v_lshl_add_u32 v182, v6, 1, v3
	s_lshl_b32 s33, s70, 7
	s_lshl_b32 s90, s70, 4
	v_lshlrev_b32_e32 v154, 1, v2
	v_lshlrev_b32_e32 v156, 1, v4
	s_movk_i32 s91, 0x7fff
	v_add_u32_e32 v183, v7, v5
	v_lshlrev_b32_e32 v242, 3, v198
	v_and_b32_e32 v240, 3, v0
	v_add_u32_e32 v241, 0xa000, v242
	v_lshlrev_b32_e32 v240, 7, v240
	v_add_u32_e32 v240, 0xa000, v240
	s_branch .LBB0_804

; __device__ __forceinline__ void sg_phase(const Frame& F, const KArgs& a, const int u_first, const int u_count) {
;     ...
;         const int s_ = tid >> 2, c0 = (tid & 3) * 32; const bf16* src = ZV + (size_t)(t0 + s_) * SGW + g * 128 + c0;
;         u32x4 zraw[4]; f32x4 lg[4][2], lb[4][2];
; #pragma unroll
;         for (int q = 0; q < 4; ++q) { zraw[q] = ((const u32x4*)src)[q];
;             lg[q][0] = *(const f32x4*)(ln_g + g * 128 + c0 + 8 * q); lg[q][1] = *(const f32x4*)(ln_g + g * 128 + c0 + 8 * q + 4); lb[q][0] = *(const f32x4*)(ln_b + g * 128 + c0 + 8 * q); lb[q][1] = *(const f32x4*)(ln_b + g * 128 + c0 + 8 * q + 4); }
;         f32x4 wraw[4][2];
; #pragma unroll
;         for (int ks = 0; ks < 4; ++ks) { const float* wp = w_sp + ((size_t)(g * 128 + t) * 128 + 32 * ks + 8 * kq); if (ks <= (w >> 1)) { wraw[ks][0] = *(const f32x4*)wp; wraw[ks][1] = *(const f32x4*)(wp + 4); } else { wraw[ks][0] = (f32x4){0.f, 0.f, 0.f, 0.f}; wraw[ks][1] = (f32x4){0.f, 0.f, 0.f, 0.f}; } }
;         u32x2 uraw[8];
; #pragma unroll
;         for (int j = 0; j < 8; ++j) uraw[j] = *(const u32x2*)(ZU + (size_t)(t0 + t) * SGW + g * 128 + 16 * j + 4 * kq);
;         const float bs = b_sp[g * 128 + t];
.LBB0_806:
	s_or_b64 exec, exec, s[70:71]
	v_add_u32_e32 v34, s76, v177
	v_ashrrev_i32_e32 v35, 31, v34
	v_lshlrev_b64 v[34:35], 11, v[34:35]
	s_and_b32 s72, s33, 0x380
	v_lshl_add_u64 v[34:35], s[80:81], 0, v[34:35]
	s_lshl_b32 s78, s72, 1
	v_lshl_add_u64 v[34:35], v[34:35], 0, s[78:79]
	v_mov_b32_e32 v155, v147
	v_lshl_add_u64 v[34:35], v[34:35], 0, v[154:155]
	s_lshl_b32 s70, s72, 2
	s_mov_b32 s71, s79
	v_lshl_add_u64 v[36:37], v[148:149], 0, s[70:71]
	v_lshl_add_u64 v[38:39], v[150:151], 0, s[70:71]
	global_load_dwordx4 v[58:61], v[34:35], off offset:48
	global_load_dwordx4 v[86:89], v[34:35], off offset:32
	global_load_dwordx4 v[110:113], v[34:35], off offset:16
	global_load_dwordx4 v[130:133], v[34:35], off
	v_readlane_b32 s98, v252, 16
	v_readlane_b32 s99, v252, 17
	v_readlane_b32 s100, v252, 18
	v_readlane_b32 s101, v252, 19
	s_add_u32 s98, s98, s70
	s_addc_u32 s99, s99, 0
	s_add_u32 s100, s100, s70
	s_addc_u32 s101, s101, 0
	global_load_dwordx2 v[244:245], v242, s[98:99]
	global_load_dwordx2 v[246:247], v242, s[100:101]
	v_add_u32_e32 v146, s72, v176
	v_lshlrev_b64 v[34:35], 9, v[146:147]
	v_lshl_add_u64 v[158:159], v[152:153], 0, v[34:35]
	global_load_dwordx4 v[62:65], v[158:159], off offset:16
	global_load_dwordx4 v[74:77], v[158:159], off
	v_cndmask_b32_e64 v34, 0, 1, s[82:83]
	v_mov_b32_e32 v42, 0
	v_cmp_ne_u32_e64 s[74:75], 1, v34
	s_andn2_b64 vcc, exec, s[82:83]
	v_mov_b32_e32 v50, 0
	v_mov_b32_e32 v51, 0
	v_mov_b32_e32 v52, 0
	v_mov_b32_e32 v53, 0
	v_mov_b32_e32 v54, 0
	v_mov_b32_e32 v55, 0
	v_mov_b32_e32 v56, 0
	v_mov_b32_e32 v57, 0
	s_cbranch_vccnz .LBB0_808
	global_load_dwordx4 v[50:53], v[158:159], off offset:144
	global_load_dwordx4 v[54:57], v[158:159], off offset:128

; __device__ __forceinline__ unsigned f2bf(float f) { unsigned u = __builtin_bit_cast(unsigned, f); return (u + 0x7fffu + ((u >> 16) & 1u)) >> 16; }
; __device__ __forceinline__ void sg_phase(const Frame& F, const KArgs& a, const int u_first, const int u_count) {
;     ...
;             lg[q][0] = *(const f32x4*)(ln_g + g * 128 + c0 + 8 * q); lg[q][1] = *(const f32x4*)(ln_g + g * 128 + c0 + 8 * q + 4); lb[q][0] = *(const f32x4*)(ln_b + g * 128 + c0 + 8 * q); lb[q][1] = *(const f32x4*)(ln_b + g * 128 + c0 + 8 * q + 4); }
;         f32x4 wraw[4][2];
; #pragma unroll
;         for (int ks = 0; ks < 4; ++ks) { const float* wp = w_sp + ((size_t)(g * 128 + t) * 128 + 32 * ks + 8 * kq); if (ks <= (w >> 1)) { wraw[ks][0] = *(const f32x4*)wp; wraw[ks][1] = *(const f32x4*)(wp + 4); } else { wraw[ks][0] = (f32x4){0.f, 0.f, 0.f, 0.f}; wraw[ks][1] = (f32x4){0.f, 0.f, 0.f, 0.f}; } }
;         u32x2 uraw[8];
; #pragma unroll
;         for (int j = 0; j < 8; ++j) uraw[j] = *(const u32x2*)(ZU + (size_t)(t0 + t) * SGW + g * 128 + 16 * j + 4 * kq);
;         const float bs = b_sp[g * 128 + t];
;         if (tid < 128) { float S = 0.f, Q = 0.f;
; #pragma unroll
;             for (int i = 0; i < 8; ++i) { const f32x4 v = zst[i]; S += v[0] + v[2]; Q += v[1] + v[3]; }
;             const float mu = S * (1.f / SGW), var = fmaxf(Q * (1.f / SGW) - mu * mu, 0.f); st[tid] = (f32x2){mu, rsqrtf(var + LN_EPS)}; }
;         __syncthreads();
;         { const int s = s_; const f32x2 ms = st[s];
; #pragma unroll
;             for (int q = 0; q < 4; ++q) { const u32x4 raw = zraw[q]; const unsigned rw[4] = {raw.x, raw.y, raw.z, raw.w};
;                 const f32x4 g0 = lg[q][0], g1 = lg[q][1], b0 = lb[q][0], b1 = lb[q][1];
; #pragma unroll
;                 for (int i = 0; i < 8; ++i) { const unsigned wd = rw[i >> 1]; const float v = __builtin_bit_cast(float, (i & 1) ? (wd & 0xffff0000u) : (wd << 16));
;                     const float gg = (i < 4) ? g0[i & 3] : g1[i & 3], bb = (i < 4) ? b0[i & 3] : b1[i & 3];
;                     vt[(c0 + 8 * q + i) * 136 + (s ^ ((tid & 3) * 16))] = (unsigned short)f2bf((v - ms[0]) * ms[1] * gg + bb); } } }
.LBB0_812:
	v_add_u32_e32 v174, s76, v176
	v_ashrrev_i32_e32 v175, 31, v174
	v_lshlrev_b64 v[158:159], 11, v[174:175]
	v_lshl_add_u64 v[158:159], s[0:1], 0, v[158:159]
	v_lshl_add_u64 v[158:159], v[158:159], 0, s[78:79]
	v_mov_b32_e32 v157, v147
	v_lshl_add_u64 v[158:159], v[158:159], 0, v[156:157]
	global_load_dwordx2 v[172:173], v[158:159], off
	global_load_dwordx2 v[170:171], v[158:159], off offset:32
	global_load_dwordx2 v[168:169], v[158:159], off offset:64
	global_load_dwordx2 v[166:167], v[158:159], off offset:96
	global_load_dwordx2 v[164:165], v[158:159], off offset:128
	global_load_dwordx2 v[162:163], v[158:159], off offset:160
	global_load_dwordx2 v[160:161], v[158:159], off offset:192
	s_nop 0
	global_load_dwordx2 v[158:159], v[158:159], off offset:224
	v_readlane_b32 s36, v252, 47
	v_readlane_b32 s37, v252, 48
	v_readlane_b32 s38, v252, 49
	v_readlane_b32 s39, v252, 50
	v_lshl_add_u64 v[184:185], v[146:147], 2, s[36:37]
	global_load_dword v146, v[184:185], off
	v_readlane_b32 s40, v252, 51
	v_readlane_b32 s41, v252, 52
	v_readlane_b32 s42, v252, 53
	v_readlane_b32 s43, v252, 54
	v_readlane_b32 s44, v252, 55
	v_readlane_b32 s45, v252, 56
	v_readlane_b32 s46, v252, 57
	v_readlane_b32 s47, v252, 58
	v_readlane_b32 s48, v252, 59
	v_readlane_b32 s49, v252, 60
	v_readlane_b32 s50, v252, 61
	v_readlane_b32 s51, v252, 62
	s_and_saveexec_b64 s[76:77], s[2:3]
	s_cbranch_execz .LBB0_814
	s_waitcnt vmcnt(21)
	v_pk_add_f32 v[184:185], v[2:3], v[4:5]
	v_pk_add_f32 v[186:187], v[6:7], v[8:9]
	v_pk_add_f32 v[184:185], v[184:185], 0 op_sel_hi:[1,0]
	s_mov_b32 s92, 0x3a800000
	v_pk_add_f32 v[184:185], v[184:185], v[186:187]
	v_pk_add_f32 v[186:187], v[10:11], v[12:13]
	s_nop 0
	v_pk_add_f32 v[184:185], v[184:185], v[186:187]
	v_pk_add_f32 v[186:187], v[14:15], v[16:17]
	s_nop 0
	v_pk_add_f32 v[184:185], v[184:185], v[186:187]
	s_waitcnt vmcnt(17)
	v_pk_add_f32 v[186:187], v[18:19], v[20:21]
	s_nop 0
	v_pk_add_f32 v[184:185], v[184:185], v[186:187]
	v_pk_add_f32 v[186:187], v[22:23], v[24:25]
	s_nop 0
	v_pk_add_f32 v[184:185], v[184:185], v[186:187]
	v_pk_add_f32 v[186:187], v[26:27], v[28:29]
	s_nop 0
	v_pk_add_f32 v[184:185], v[184:185], v[186:187]
	v_pk_add_f32 v[186:187], v[30:31], v[32:33]
	s_nop 0
	v_pk_add_f32 v[184:185], v[184:185], v[186:187]
	s_nop 0
	v_pk_mul_f32 v[184:185], v[184:185], s[92:93] op_sel_hi:[1,0]
	s_mov_b32 s92, 0x800000
	v_fma_f32 v155, -v184, v184, v185
	v_max_f32_e32 v155, 0, v155
	v_add_f32_e32 v155, 0x3727c5ac, v155
	v_mul_f32_e32 v157, 0x4b800000, v155
	v_cmp_gt_f32_e32 vcc, s92, v155
	s_nop 1
	v_cndmask_b32_e32 v155, v155, v157, vcc
	v_rsq_f32_e32 v155, v155
	s_nop 0
	v_mul_f32_e32 v157, 0x45800000, v155
	v_cndmask_b32_e32 v185, v155, v157, vcc
	ds_write_b64 v178, v[184:185]
.LBB0_814:
	s_or_b64 exec, exec, s[76:77]
	s_waitcnt vmcnt(11)
	ds_write_b64 v241, v[244:245]
	ds_write_b64 v241, v[246:247] offset:1024
	s_waitcnt lgkmcnt(0)
	s_barrier
	ds_read_b128 v[138:141], v240
	ds_read_b128 v[126:129], v240 offset:16
	ds_read_b128 v[118:121], v240 offset:32
	ds_read_b128 v[106:109], v240 offset:48
	ds_read_b128 v[98:101], v240 offset:64
	ds_read_b128 v[90:93], v240 offset:80
	ds_read_b128 v[78:81], v240 offset:96
	ds_read_b128 v[66:69], v240 offset:112
	ds_read_b128 v[142:145], v240 offset:1024
	ds_read_b128 v[134:137], v240 offset:1040
	ds_read_b128 v[122:125], v240 offset:1056
	ds_read_b128 v[114:117], v240 offset:1072
	ds_read_b128 v[102:105], v240 offset:1088
	ds_read_b128 v[94:97], v240 offset:1104
	ds_read_b128 v[82:85], v240 offset:1120
	ds_read_b128 v[70:73], v240 offset:1136
	ds_read_b64 v[184:185], v179
	s_waitcnt vmcnt(13)
	v_lshlrev_b32_e32 v155, 16, v130
	v_and_b32_e32 v130, 0xffff0000, v130
	s_waitcnt vmcnt(10)
	v_cndmask_b32_e64 v62, v62, 0, s[12:13]
	v_cndmask_b32_e64 v63, v63, 0, s[14:15]
	s_waitcnt lgkmcnt(0)
	v_sub_f32_e32 v155, v155, v184
	v_mul_f32_e32 v155, v185, v155
	v_fma_f32 v138, v138, v155, v142
	v_sub_f32_e32 v130, v130, v184
	v_bfe_u32 v142, v138, 16, 1
	v_mul_f32_e32 v130, v185, v130
	v_add3_u32 v138, v138, v142, s91
	v_fma_f32 v130, v139, v130, v143
	ds_write_b16_d16_hi v183, v138 offset:1024
	v_bfe_u32 v138, v130, 16, 1
	v_add3_u32 v130, v130, v138, s91
	ds_write_b16_d16_hi v183, v130 offset:1296
	v_lshlrev_b32_e32 v130, 16, v131
	v_sub_f32_e32 v130, v130, v184
	v_mul_f32_e32 v130, v185, v130
	v_fma_f32 v130, v140, v130, v144
	v_bfe_u32 v138, v130, 16, 1
	v_add3_u32 v130, v130, v138, s91
	ds_write_b16_d16_hi v183, v130 offset:1568
	v_and_b32_e32 v130, 0xffff0000, v131
	v_sub_f32_e32 v130, v130, v184
	v_mul_f32_e32 v130, v185, v130
	v_fmac_f32_e32 v145, v141, v130
	v_bfe_u32 v130, v145, 16, 1
	v_add3_u32 v130, v145, v130, s91
	ds_write_b16_d16_hi v183, v130 offset:1840
	v_lshlrev_b32_e32 v130, 16, v132
	v_sub_f32_e32 v130, v130, v184
	v_mul_f32_e32 v130, v185, v130
	v_fma_f32 v126, v126, v130, v134
	v_bfe_u32 v130, v126, 16, 1
	v_add3_u32 v126, v126, v130, s91
	ds_write_b16_d16_hi v183, v126 offset:2112
	v_and_b32_e32 v126, 0xffff0000, v132
	v_sub_f32_e32 v126, v126, v184
	v_mul_f32_e32 v126, v185, v126
	v_fma_f32 v126, v127, v126, v135
	v_bfe_u32 v127, v126, 16, 1
	v_add3_u32 v126, v126, v127, s91
	ds_write_b16_d16_hi v183, v126 offset:2384
	v_lshlrev_b32_e32 v126, 16, v133
	v_sub_f32_e32 v126, v126, v184
	v_mul_f32_e32 v126, v185, v126
	v_fma_f32 v126, v128, v126, v136
	v_bfe_u32 v127, v126, 16, 1
	v_add3_u32 v126, v126, v127, s91
	ds_write_b16_d16_hi v183, v126 offset:2656
	v_and_b32_e32 v126, 0xffff0000, v133
	v_sub_f32_e32 v126, v126, v184
	v_mul_f32_e32 v126, v185, v126
	v_fmac_f32_e32 v137, v129, v126
	v_bfe_u32 v126, v137, 16, 1
	v_add3_u32 v126, v137, v126, s91
; __device__ __forceinline__ unsigned f2bf(float f) { unsigned u = __builtin_bit_cast(unsigned, f); return (u + 0x7fffu + ((u >> 16) & 1u)) >> 16; }
; __device__ __forceinline__ void sg_phase(const Frame& F, const KArgs& a, const int u_first, const int u_count) {
;     ...
;         { const int s = s_; const f32x2 ms = st[s];
; #pragma unroll
;             for (int q = 0; q < 4; ++q) { const u32x4 raw = zraw[q]; const unsigned rw[4] = {raw.x, raw.y, raw.z, raw.w};
;                 const f32x4 g0 = lg[q][0], g1 = lg[q][1], b0 = lb[q][0], b1 = lb[q][1];
; #pragma unroll
;                 for (int i = 0; i < 8; ++i) { const unsigned wd = rw[i >> 1]; const float v = __builtin_bit_cast(float, (i & 1) ? (wd & 0xffff0000u) : (wd << 16));
;                     const float gg = (i < 4) ? g0[i & 3] : g1[i & 3], bb = (i < 4) ? b0[i & 3] : b1[i & 3];
;                     vt[(c0 + 8 * q + i) * 136 + (s ^ ((tid & 3) * 16))] = (unsigned short)f2bf((v - ms[0]) * ms[1] * gg + bb); } } }
;         __syncthreads();
;         f32x4 acc[8];
; #pragma unroll
;         for (int j = 0; j < 8; ++j) acc[j] = (f32x4){0.f, 0.f, 0.f, 0.f};
; #pragma unroll
;         for (int ks = 0; ks < 4; ++ks) { if (ks > (w >> 1)) continue;
;             const f32x4 w0 = wraw[ks][0], w1 = wraw[ks][1];
;             float wv[8] = {w0[0], w0[1], w0[2], w0[3], w1[0], w1[1], w1[2], w1[3]};
; #pragma unroll
;             for (int i = 0; i < 8; ++i) if (32 * ks + 8 * kq + i > t) wv[i] = 0.f;
	ds_write_b16_d16_hi v183, v126 offset:2928
	v_lshlrev_b32_e32 v126, 16, v110
	v_sub_f32_e32 v126, v126, v184
	v_mul_f32_e32 v126, v185, v126
	v_and_b32_e32 v110, 0xffff0000, v110
	v_fma_f32 v118, v118, v126, v122
	v_sub_f32_e32 v110, v110, v184
	v_bfe_u32 v122, v118, 16, 1
	v_mul_f32_e32 v110, v185, v110
	v_add3_u32 v118, v118, v122, s91
	v_fma_f32 v110, v119, v110, v123
	ds_write_b16_d16_hi v183, v118 offset:3200
	v_bfe_u32 v118, v110, 16, 1
	v_add3_u32 v110, v110, v118, s91
	ds_write_b16_d16_hi v183, v110 offset:3472
	v_lshlrev_b32_e32 v110, 16, v111
	v_sub_f32_e32 v110, v110, v184
	v_mul_f32_e32 v110, v185, v110
	v_fma_f32 v110, v120, v110, v124
	v_bfe_u32 v118, v110, 16, 1
	v_add3_u32 v110, v110, v118, s91
	ds_write_b16_d16_hi v183, v110 offset:3744
	v_and_b32_e32 v110, 0xffff0000, v111
	v_sub_f32_e32 v110, v110, v184
	v_mul_f32_e32 v110, v185, v110
	v_fmac_f32_e32 v125, v121, v110
	v_bfe_u32 v110, v125, 16, 1
	v_add3_u32 v110, v125, v110, s91
	ds_write_b16_d16_hi v183, v110 offset:4016
	v_lshlrev_b32_e32 v110, 16, v112
	v_sub_f32_e32 v110, v110, v184
	v_mul_f32_e32 v110, v185, v110
	v_fma_f32 v106, v106, v110, v114
	v_bfe_u32 v110, v106, 16, 1
	v_add3_u32 v106, v106, v110, s91
	ds_write_b16_d16_hi v183, v106 offset:4288
	v_and_b32_e32 v106, 0xffff0000, v112
	v_sub_f32_e32 v106, v106, v184
	v_mul_f32_e32 v106, v185, v106
	v_fma_f32 v106, v107, v106, v115
	v_bfe_u32 v107, v106, 16, 1
	v_add3_u32 v106, v106, v107, s91
	ds_write_b16_d16_hi v183, v106 offset:4560
	v_lshlrev_b32_e32 v106, 16, v113
	v_sub_f32_e32 v106, v106, v184
	v_mul_f32_e32 v106, v185, v106
	v_fma_f32 v106, v108, v106, v116
	v_bfe_u32 v107, v106, 16, 1
	v_add3_u32 v106, v106, v107, s91
	ds_write_b16_d16_hi v183, v106 offset:4832
	v_and_b32_e32 v106, 0xffff0000, v113
	v_sub_f32_e32 v106, v106, v184
	v_mul_f32_e32 v106, v185, v106
	v_fmac_f32_e32 v117, v109, v106
	v_bfe_u32 v106, v117, 16, 1
	v_add3_u32 v106, v117, v106, s91
	ds_write_b16_d16_hi v183, v106 offset:5104
	v_lshlrev_b32_e32 v106, 16, v86
	v_sub_f32_e32 v106, v106, v184
	v_mul_f32_e32 v106, v185, v106
	v_and_b32_e32 v86, 0xffff0000, v86
	v_fma_f32 v98, v98, v106, v102
	v_sub_f32_e32 v86, v86, v184
	v_bfe_u32 v102, v98, 16, 1
	v_mul_f32_e32 v86, v185, v86
	v_add3_u32 v98, v98, v102, s91
	v_fma_f32 v86, v99, v86, v103
	ds_write_b16_d16_hi v183, v98 offset:5376
	v_bfe_u32 v98, v86, 16, 1
	v_add3_u32 v86, v86, v98, s91
	ds_write_b16_d16_hi v183, v86 offset:5648
	v_lshlrev_b32_e32 v86, 16, v87
	v_sub_f32_e32 v86, v86, v184
	v_mul_f32_e32 v86, v185, v86
	v_fma_f32 v86, v100, v86, v104
	v_bfe_u32 v98, v86, 16, 1
	v_add3_u32 v86, v86, v98, s91
	ds_write_b16_d16_hi v183, v86 offset:5920
	v_and_b32_e32 v86, 0xffff0000, v87
	v_sub_f32_e32 v86, v86, v184
	v_mul_f32_e32 v86, v185, v86
	v_fmac_f32_e32 v105, v101, v86
	v_bfe_u32 v86, v105, 16, 1
	v_add3_u32 v86, v105, v86, s91
	ds_write_b16_d16_hi v183, v86 offset:6192
	v_lshlrev_b32_e32 v86, 16, v88
	v_sub_f32_e32 v86, v86, v184
	v_mul_f32_e32 v86, v185, v86
	v_fma_f32 v86, v90, v86, v94
	v_bfe_u32 v87, v86, 16, 1
	v_add3_u32 v86, v86, v87, s91
	ds_write_b16_d16_hi v183, v86 offset:6464
	v_and_b32_e32 v86, 0xffff0000, v88
	v_sub_f32_e32 v86, v86, v184
	v_mul_f32_e32 v86, v185, v86
	v_fma_f32 v86, v91, v86, v95
	v_bfe_u32 v87, v86, 16, 1
	v_add3_u32 v86, v86, v87, s91
	ds_write_b16_d16_hi v183, v86 offset:6736
	v_lshlrev_b32_e32 v86, 16, v89
	v_sub_f32_e32 v86, v86, v184
	v_mul_f32_e32 v86, v185, v86
	v_fma_f32 v86, v92, v86, v96
	v_bfe_u32 v87, v86, 16, 1
	v_add3_u32 v86, v86, v87, s91
	ds_write_b16_d16_hi v183, v86 offset:7008
	v_and_b32_e32 v86, 0xffff0000, v89
	v_sub_f32_e32 v86, v86, v184
	v_mul_f32_e32 v86, v185, v86
	v_fmac_f32_e32 v97, v93, v86
	v_bfe_u32 v86, v97, 16, 1
	v_add3_u32 v86, v97, v86, s91
	ds_write_b16_d16_hi v183, v86 offset:7280
	v_lshlrev_b32_e32 v86, 16, v58
	v_sub_f32_e32 v86, v86, v184
	v_mul_f32_e32 v86, v185, v86
	v_and_b32_e32 v58, 0xffff0000, v58
	v_fma_f32 v78, v78, v86, v82
	v_sub_f32_e32 v58, v58, v184
	v_bfe_u32 v82, v78, 16, 1
	v_mul_f32_e32 v58, v185, v58
	v_add3_u32 v78, v78, v82, s91
	v_fma_f32 v58, v79, v58, v83
	ds_write_b16_d16_hi v183, v78 offset:7552
	v_bfe_u32 v78, v58, 16, 1
	v_add3_u32 v58, v58, v78, s91
	ds_write_b16_d16_hi v183, v58 offset:7824
	v_lshlrev_b32_e32 v58, 16, v59
	v_sub_f32_e32 v58, v58, v184
	v_mul_f32_e32 v58, v185, v58
	v_fma_f32 v58, v80, v58, v84
	v_bfe_u32 v78, v58, 16, 1
	v_add3_u32 v58, v58, v78, s91
	ds_write_b16_d16_hi v183, v58 offset:8096
	v_and_b32_e32 v58, 0xffff0000, v59
	v_sub_f32_e32 v58, v58, v184
	v_mul_f32_e32 v58, v185, v58
	v_fmac_f32_e32 v85, v81, v58
	v_bfe_u32 v58, v85, 16, 1
	v_add3_u32 v58, v85, v58, s91
	ds_write_b16_d16_hi v183, v58 offset:8368
	v_lshlrev_b32_e32 v58, 16, v60
	v_sub_f32_e32 v58, v58, v184
	v_mul_f32_e32 v58, v185, v58
	v_fma_f32 v58, v66, v58, v70
	v_bfe_u32 v59, v58, 16, 1
	v_add3_u32 v58, v58, v59, s91
	ds_write_b16_d16_hi v183, v58 offset:8640
	v_and_b32_e32 v58, 0xffff0000, v60
	v_sub_f32_e32 v58, v58, v184
	v_mul_f32_e32 v58, v185, v58
	v_fma_f32 v58, v67, v58, v71
	v_bfe_u32 v59, v58, 16, 1
	v_add3_u32 v58, v58, v59, s91
	ds_write_b16_d16_hi v183, v58 offset:8912
	v_lshlrev_b32_e32 v58, 16, v61
	v_sub_f32_e32 v58, v58, v184
	v_mul_f32_e32 v58, v185, v58
	v_fma_f32 v58, v68, v58, v72
	v_bfe_u32 v59, v58, 16, 1
	v_add3_u32 v58, v58, v59, s91
	ds_write_b16_d16_hi v183, v58 offset:9184
	v_and_b32_e32 v58, 0xffff0000, v61
	v_sub_f32_e32 v58, v58, v184
	v_mul_f32_e32 v58, v185, v58
	v_fmac_f32_e32 v73, v69, v58
	v_bfe_u32 v58, v73, 16, 1
	v_add3_u32 v58, v73, v58, s91
	ds_write_b16_d16_hi v183, v58 offset:9456
	s_waitcnt vmcnt(9)
	v_cndmask_b32_e64 v58, v74, 0, s[4:5]
	v_cndmask_b32_e64 v59, 0, v75, s[6:7]
	v_cndmask_b32_e64 v58, v58, v74, s[6:7]
	v_cndmask_b32_e64 v60, v76, 0, s[8:9]
	v_cndmask_b32_e64 v61, v77, 0, s[10:11]
	v_cndmask_b32_e64 v64, v64, 0, s[16:17]
	v_cndmask_b32_e64 v65, v65, 0, s[18:19]
	s_waitcnt lgkmcnt(0)
	s_barrier
; #define LAS __attribute__((address_space(3)))
; __device__ __forceinline__ unsigned cvt_pk_bf16(float lo, float hi) { unsigned r; asm volatile("v_cvt_pk_bf16_f32 %0, %1, %2" : "=v"(r) : "v"(lo), "v"(hi)); return r; }
; __device__ __forceinline__ void sg_phase(const Frame& F, const KArgs& a, const int u_first, const int u_count) {
;     ...
;         for (int ks = 0; ks < 4; ++ks) { if (ks > (w >> 1)) continue;
;             const f32x4 w0 = wraw[ks][0], w1 = wraw[ks][1];
;             float wv[8] = {w0[0], w0[1], w0[2], w0[3], w1[0], w1[1], w1[2], w1[3]};
; #pragma unroll
;             for (int i = 0; i < 8; ++i) if (32 * ks + 8 * kq + i > t) wv[i] = 0.f;
;             u32x4 pk; pk.x = cvt_pk_bf16(wv[0], wv[1]); pk.y = cvt_pk_bf16(wv[2], wv[3]); pk.z = cvt_pk_bf16(wv[4], wv[5]); pk.w = cvt_pk_bf16(wv[6], wv[7]);
;             const bf16x8 wf = __builtin_bit_cast(bf16x8, pk);
; #pragma unroll
;             for (int j = 0; j < 8; ++j) { const bf16x8 vf = *(const LAS bf16x8*)(vt + (16 * j + tl) * 136 + ((32 * ks + 8 * kq) ^ ((j >> 1) * 16)));
;                 acc[j] = __builtin_amdgcn_mfma_f32_16x16x32_bf16(vf, wf, acc[j], 0, 0, 0); }
;         }
	v_cvt_pk_bf16_f32 v58, v58, v59
	v_cvt_pk_bf16_f32 v59, v60, v61
	v_cvt_pk_bf16_f32 v60, v62, v63
	v_cvt_pk_bf16_f32 v61, v64, v65
	ds_read_b128 v[62:65], v180 offset:1024
	ds_read_b128 v[66:69], v180 offset:5376
	s_waitcnt lgkmcnt(1)
	v_mfma_f32_16x16x32_bf16 v[86:89], v[62:65], v[58:61], 0
	ds_read_b128 v[62:65], v181 offset:9728
	ds_read_b128 v[90:93], v181 offset:31552
	s_and_b64 vcc, exec, s[74:75]
	s_waitcnt lgkmcnt(2)
	v_mfma_f32_16x16x32_bf16 v[82:85], v[66:69], v[58:61], 0
	ds_read_b128 v[66:69], v181 offset:14080
	s_waitcnt lgkmcnt(2)
	v_mfma_f32_16x16x32_bf16 v[78:81], v[62:65], v[58:61], 0
	ds_read_b128 v[62:65], v180 offset:18496
	s_waitcnt lgkmcnt(1)
	v_mfma_f32_16x16x32_bf16 v[74:77], v[66:69], v[58:61], 0
	ds_read_b128 v[66:69], v180 offset:22848
	s_waitcnt lgkmcnt(1)
	v_mfma_f32_16x16x32_bf16 v[70:73], v[62:65], v[58:61], 0
	ds_read_b128 v[62:65], v181 offset:27200
	s_waitcnt lgkmcnt(1)
	v_mfma_f32_16x16x32_bf16 v[66:69], v[66:69], v[58:61], 0
	s_waitcnt lgkmcnt(0)
	v_mfma_f32_16x16x32_bf16 v[62:65], v[62:65], v[58:61], 0
	v_mfma_f32_16x16x32_bf16 v[58:61], v[90:93], v[58:61], 0
	s_cbranch_vccnz .LBB0_816
	v_readlane_b32 s36, v251, 7
	v_readlane_b32 s37, v251, 8
	v_cndmask_b32_e64 v53, v53, 0, s[94:95]
	v_cndmask_b32_e64 v92, v52, 0, s[34:35]
	v_cndmask_b32_e64 v54, v54, 0, s[36:37]
	v_readlane_b32 s36, v251, 16
	v_readlane_b32 s37, v251, 17
	s_nop 1
	v_cndmask_b32_e64 v55, v55, 0, s[36:37]
	v_readlane_b32 s36, v251, 22
	v_readlane_b32 s37, v251, 23
	s_nop 1
	v_cndmask_b32_e64 v56, v56, 0, s[36:37]
	v_readlane_b32 s36, v251, 24
	v_readlane_b32 s37, v251, 25
	s_nop 1
	v_cndmask_b32_e64 v57, v57, 0, s[36:37]
	v_readlane_b32 s36, v251, 26
	v_readlane_b32 s37, v251, 27
	s_nop 1
	v_cndmask_b32_e64 v90, v50, 0, s[36:37]
	v_readlane_b32 s36, v251, 28
	v_readlane_b32 s37, v251, 29
	v_cvt_pk_bf16_f32 v50, v54, v55
	s_nop 1
	v_cndmask_b32_e64 v91, v51, 0, s[36:37]
	v_cvt_pk_bf16_f32 v51, v56, v57
	v_cvt_pk_bf16_f32 v52, v90, v91
	v_cvt_pk_bf16_f32 v53, v92, v53
	ds_read_b128 v[2:5], v180 offset:1088
	ds_read_b128 v[6:9], v180 offset:5440
	ds_read_b128 v[10:13], v181 offset:9792
	ds_read_b128 v[14:17], v181 offset:14144
	ds_read_b128 v[18:21], v180 offset:18432
	ds_read_b128 v[22:25], v180 offset:22784
	ds_read_b128 v[26:29], v181 offset:27136
	ds_read_b128 v[30:33], v181 offset:31488
	s_waitcnt lgkmcnt(7)
	v_mfma_f32_16x16x32_bf16 v[86:89], v[2:5], v[50:53], v[86:89]
	s_waitcnt lgkmcnt(6)
	v_mfma_f32_16x16x32_bf16 v[82:85], v[6:9], v[50:53], v[82:85]
	s_waitcnt lgkmcnt(5)
	v_mfma_f32_16x16x32_bf16 v[78:81], v[10:13], v[50:53], v[78:81]
	s_waitcnt lgkmcnt(4)
	v_mfma_f32_16x16x32_bf16 v[74:77], v[14:17], v[50:53], v[74:77]
	s_waitcnt lgkmcnt(3)
	v_mfma_f32_16x16x32_bf16 v[70:73], v[18:21], v[50:53], v[70:73]
	s_waitcnt lgkmcnt(2)
	v_mfma_f32_16x16x32_bf16 v[66:69], v[22:25], v[50:53], v[66:69]
	s_waitcnt lgkmcnt(1)
	v_mfma_f32_16x16x32_bf16 v[62:65], v[26:29], v[50:53], v[62:65]
	s_waitcnt lgkmcnt(0)
	v_mfma_f32_16x16x32_bf16 v[58:61], v[30:33], v[50:53], v[58:61]
